# scans-mixers grid barrier split: release+counter after scans, acquire poll before first consumer unit (attention/conversion no longer wait)
# speedup vs baseline: 1.0085x; 1.0058x over previous
; __device__ __forceinline__ unsigned xb_ld(unsigned* p)              { return __hip_atomic_load(p, __ATOMIC_RELAXED, __HIP_MEMORY_SCOPE_AGENT); }
; __device__ __forceinline__ unsigned xb_add(unsigned* p, unsigned v) { return __hip_atomic_fetch_add(p, v, __ATOMIC_RELAXED, __HIP_MEMORY_SCOPE_AGENT); }
; #define XB_SPIN(cond, bar) do { unsigned _sp = 0; while (cond) { __builtin_amdgcn_s_sleep(1); \
;     if ((++_sp & 255u) == 0u) { if (xb_ld(&(bar)[XB_TMO])) break; if (_sp > XB_SPIN_CAP) { atomicAdd(&(bar)[XB_TMO], 1u); break; } } } } while (0)
; __device__ __forceinline__ void xcd_barrier(const XcdBarrier& b) {
;     asm volatile("s_waitcnt vmcnt(0)" ::: "memory");
;     __syncthreads();
;     if (threadIdx.x == 0) {
;         unsigned* bar = b.bar;
;         __builtin_amdgcn_s_waitcnt(0);
;         unsigned nloc = b.st[0], nx = b.st[1];
;         if (nloc == 0u) { xcd_barrier_complete(bar, b.x, nloc, nx); b.st[0] = nloc; b.st[1] = nx; }
;         const unsigned old = xb_add(&bar[XB_XSUB(b.x)], 1u);
;         const unsigned gen = old / nloc;
;         if (old + 1u == (gen + 1u) * nloc) {
;             __builtin_amdgcn_fence(__ATOMIC_RELEASE, XB_SCOPE);
;             asm volatile("s_waitcnt vmcnt(0)" ::: "memory");
;             const unsigned og = xb_add(&bar[XB_TOP], 1u);
;             const unsigned tg = og / nx;
;             if (og + 1u == (tg + 1u) * nx) xb_add(&bar[XB_TOPGEN], 1u);
;             else XB_SPIN(xb_ld(&bar[XB_TOPGEN]) == tg, bar);
;             __builtin_amdgcn_fence(__ATOMIC_ACQUIRE, XB_SCOPE);
;             xb_add(&bar[XB_XGEN(b.x)], 1u);
;             asm volatile("s_waitcnt vmcnt(0)" ::: "memory");
;         } else {
;             XB_SPIN(xb_ld(&bar[XB_XGEN(b.x)]) == gen, bar);
;             __builtin_amdgcn_fence(__ATOMIC_ACQUIRE, XB_SCOPE);
;             asm volatile("s_waitcnt vmcnt(0)" ::: "memory");
;         }
;     }
;     __syncthreads();
; }
; __global__ void __launch_bounds__(NWAVES * 64, 2) mega_fwd(Args args) {
;     ...
;             if (F.wave < 4) { p_scans(F); if (!CV_IN_MIX) p_convert(F, F.l, cv0_, CV_ALL); if (!mixhead_ && F.l + 1 < NLAYER) p_convert(F, F.l + 1, 0, CV_WIN); }
;             else { if (!CV_IN_MIX) p_convert(F, F.l, cv0_, CV_ALL); if (!mixhead_ && F.l + 1 < NLAYER) p_convert(F, F.l + 1, 0, CV_WIN); p_scans(F); } }
;         SEAM();
.LBB0_2163:
	v_readlane_b32 s2, v255, 14
	s_add_i32 s50, s2, 4
	v_readlane_b32 s2, v255, 10
	v_readlane_b32 s3, v255, 11
	s_cmp_lt_i32 s50, s3
	s_cselect_b64 s[2:3], -1, 0
	s_and_b64 s[0:1], s[0:1], s[2:3]
	s_andn2_b64 vcc, exec, s[0:1]
	s_waitcnt vmcnt(0) lgkmcnt(0)
	s_barrier
	s_mov_b64 s[4:5], exec
	v_readlane_b32 s10, v255, 8
	v_readlane_b32 s11, v255, 9
	s_nop 3
	s_and_b64 s[10:11], s[4:5], s[10:11]
	s_mov_b64 exec, s[10:11]
	s_cbranch_execz .Lmy_s4a_done
	buffer_wbl2 sc0 sc1
	s_waitcnt vmcnt(0)
	v_readlane_b32 s12, v255, 5
	v_readlane_b32 s13, v255, 6
	s_nop 3
	v_mov_b32_e32 v0, 0xb000
	v_mov_b32_e32 v1, 1
	global_atomic_add v0, v1, s[12:13]
	s_waitcnt vmcnt(0)
.Lmy_s4a_done:
	s_mov_b64 exec, s[4:5]
	s_branch .LBB0_2217

; #define CV_PIECE() do { if (cvp < CVJ) { __syncthreads(); refresh(F); p_convert_np(F, F.l, CV_DENSE, CV_ALL, (F.vcu * NWAVES + F.wave) * CVJ + cvp, F.G * NWAVES * CVJ); ++cvp; __syncthreads(); } } while (0)
; __global__ void __launch_bounds__(NWAVES * 64, 2) mega_fwd(Args args) {
;     ...
;             } else if (QMODE >= 3) {
;                 for (;;) {
;                     if (F.tid == 0) QS[0] = (int)__hip_atomic_fetch_add(F.ctl + CW_Q + 64 * F.l + 32, 1u, __ATOMIC_RELAXED, __HIP_MEMORY_SCOPE_AGENT);
;                     __syncthreads();
;                     const int j = __builtin_amdgcn_readfirstlane(QS[0]);
;                     __syncthreads();
;                     if (j >= (QMODE == 4 ? 512 : 1024)) break;
;                     if (QMODE == 3) { SgPre P_; sg_load(F, j >> 2, j & 3, P_); sg_unit(F, F.l, j >> 2, j & 3, P_); } else if (QMODE == 4) ssd_out_unit(F, F.l, j >> 1, j & 1); else { MlPre P_; ml_out_load(F, j >> 2, j & 3, P_); ml_out_unit(F, F.l, j >> 2, j & 3, P_); }
;                     CV_PIECE();
;                 }
.LBB0_2845:
	s_mov_b64 s[26:27], exec
	v_cmp_eq_u32_e32 vcc, 0, v130
	s_and_b64 exec, exec, vcc
	s_cbranch_execz .Lmy_s4w_done
	s_add_u32 s28, s10, 0xb000
	s_addc_u32 s29, s11, 0
	s_add_i32 s30, s8, 1
	s_lshl_b32 s30, s30, 8
	s_mov_b32 s32, 0
	v_mov_b32_e32 v0, 0
.Lmy_s4w_spin:
	global_load_dword v1, v0, s[28:29] sc1
	s_waitcnt vmcnt(0)
	v_cmp_gt_u32_e32 vcc, s30, v1
	s_cbranch_vccz .Lmy_s4w_ok
	s_sleep 1
	s_add_i32 s32, s32, 1
	s_cmp_lt_u32 s32, 0x400000
	s_cbranch_scc1 .Lmy_s4w_spin
.Lmy_s4w_ok:
	buffer_inv sc0 sc1
	s_waitcnt vmcnt(0)
.Lmy_s4w_done:
	s_mov_b64 exec, s[26:27]
	s_waitcnt vmcnt(0) lgkmcnt(0)
	s_barrier
	s_add_u32 s0, s10, s12
	s_addc_u32 s1, s11, s13
	s_add_u32 s24, s0, 0x9080
	s_addc_u32 s25, s1, 0
	s_lshl_b32 s22, s8, 2
	v_cmp_eq_u32_e32 vcc, 0, v130
	s_and_saveexec_b64 s[0:1], vcc
	s_cbranch_execz .LBB0_2849
